# P3 epilogue: first two residual rows of the second batch (8 loads) issued right behind the first batch's loads into spare registers; batch-1 counted waits +8
# speedup vs baseline: 1.0016x; 1.0016x over previous
; __device__ __forceinline__ unsigned cvt_pk_bf16(float lo, float hi) { unsigned r; asm volatile("v_cvt_pk_bf16_f32 %0, %1, %2" : "=v"(r) : "v"(lo), "v"(hi)); return r; }
;     __device__ __forceinline__ void operator()(const f32x4 (&acc)[2][2][4][2], const pg8::Unit& u, int wr, int wc, int fr, int fq) const {
;         const int row0 = u.pm * 256 + wr * 64 + fr, col0 = u.pn * 256 + wc * 64 + 16 * fq;
; #pragma unroll
;         for (int ai = 0; ai < 2; ++ai) {
;             f32x4 b0[4][2], b1[4][2];
; #pragma unroll
;             for (int m = 0; m < 4; ++m)
; #pragma unroll
;                 for (int bj = 0; bj < 2; ++bj) { const size_t off = (size_t)(row0 + ai * 128 + m * 16) * D + col0 + bj * 8;
;                     if (BASE_F32) { b0[m][bj] = *(const f32x4*)((const float*)base + off); b1[m][bj] = *(const f32x4*)((const float*)base + off + 4); }
;                     else { const u32x4 w = *(const u32x4*)((const bf16*)base + off); b0[m][bj] = (f32x4){bflo(w.x), bfhi(w.x), bflo(w.y), bfhi(w.y)}; b1[m][bj] = (f32x4){bflo(w.z), bfhi(w.z), bflo(w.w), bfhi(w.w)}; } }
;             asm volatile("" ::: "memory");
; #pragma unroll
;             for (int m = 0; m < 4; ++m) { const int row = row0 + ai * 128 + m * 16; float ss = 0.f;
;                 u32x4 q;
; #pragma unroll
;                 for (int bj = 0; bj < 2; ++bj) { const size_t off = (size_t)row * D + col0 + bj * 8;
;                     const float asc = BASE_F32 ? 1.0f : (1.0f / 256.0f);
;                     const f32x4 v0 = acc[ai][bj][m][0] * asc + b0[m][bj], v1 = acc[ai][bj][m][1] * asc + b1[m][bj];
;                     ss += (v0[0] * v0[0] + v0[1] * v0[1]) + (v0[2] * v0[2] + v0[3] * v0[3]) + (v1[0] * v1[0] + v1[1] * v1[1]) + (v1[2] * v1[2] + v1[3] * v1[3]);
;                     u32x4 w; w.x = cvt_pk_bf16(v0[0], v0[1]); w.y = cvt_pk_bf16(v0[2], v0[3]); w.z = cvt_pk_bf16(v1[0], v1[1]); w.w = cvt_pk_bf16(v1[2], v1[3]);
;                     *(u32x4*)(out + off) = w;
;                     if (BASE_F32) { const unsigned qa = pk4_fp8(v0[0], v0[1], v0[2], v0[3]), qb = pk4_fp8(v1[0], v1[1], v1[2], v1[3]); if (bj == 0) { q.x = qa; q.y = qb; } else { q.z = qa; q.w = qb; } } }
;                 if (BASE_F32) *(u32x4*)(q8 + (size_t)row * D + col0) = q;
;                 ss += __shfl_xor(ss, 16); ss += __shfl_xor(ss, 32);
;                 if (fq == 0) ssq[(size_t)row * 16 + u.pn * 4 + wc] = ss; }
.LBB0_554:
	s_lshl_b32 s2, s19, 8
	v_mov_b32_e32 v130, v0
	s_add_i32 s2, s2, s42
	v_mov_b32_e32 v214, 0
	v_and_or_b32 v182, v130, 15, s2
	s_lshl_b32 s2, s15, 8
	v_bfe_u32 v179, v130, 4, 2
	s_or_b32 s2, s2, s43
	v_lshl_or_b32 v180, v179, 4, s2
	v_ashrrev_i32_e32 v181, 31, v180
	v_ashrrev_i32_e32 v183, 31, v182
	v_lshl_add_u64 v[184:185], v[180:181], 2, s[16:17]
	v_lshlrev_b64 v[130:131], 12, v[182:183]
	v_lshl_add_u64 v[130:131], v[184:185], 0, v[130:131]
	global_load_dwordx4 v[198:201], v[130:131], off
	global_load_dwordx4 v[202:205], v[130:131], off offset:16
	global_load_dwordx4 v[206:209], v[130:131], off offset:32
	global_load_dwordx4 v[210:213], v[130:131], off offset:48
	v_or_b32_e32 v190, 16, v182
	v_or_b32_e32 v188, 32, v182
	v_or_b32_e32 v186, 48, v182
	v_ashrrev_i32_e32 v191, 31, v190
	v_ashrrev_i32_e32 v189, 31, v188
	v_ashrrev_i32_e32 v187, 31, v186
	v_lshlrev_b64 v[130:131], 12, v[190:191]
	v_lshlrev_b64 v[132:133], 12, v[188:189]
	v_lshlrev_b64 v[134:135], 12, v[186:187]
	v_lshl_add_u64 v[130:131], v[184:185], 0, v[130:131]
	v_lshl_add_u64 v[132:133], v[184:185], 0, v[132:133]
	v_lshl_add_u64 v[142:143], v[184:185], 0, v[134:135]
	global_load_dwordx4 v[162:165], v[130:131], off offset:48
	global_load_dwordx4 v[166:169], v[130:131], off offset:32
	global_load_dwordx4 v[170:173], v[130:131], off offset:16
	global_load_dwordx4 v[174:177], v[130:131], off
	global_load_dwordx4 v[146:149], v[132:133], off offset:48
	global_load_dwordx4 v[150:153], v[132:133], off offset:32
	global_load_dwordx4 v[154:157], v[132:133], off offset:16
	global_load_dwordx4 v[158:161], v[132:133], off
	s_nop 0
	global_load_dwordx4 v[130:133], v[142:143], off offset:48
	global_load_dwordx4 v[134:137], v[142:143], off offset:32
	global_load_dwordx4 v[138:141], v[142:143], off offset:16
	s_nop 0
	global_load_dwordx4 v[142:145], v[142:143], off
	s_mov_b64 s[98:99], 0x80000
	v_lshlrev_b64 v[252:253], 12, v[182:183]
	v_lshl_add_u64 v[252:253], v[184:185], 0, v[252:253]
	v_lshl_add_u64 v[252:253], v[252:253], 0, s[98:99]
	global_load_dwordx4 v[220:223], v[252:253], off
	global_load_dwordx4 v[224:227], v[252:253], off offset:16
	global_load_dwordx4 v[228:231], v[252:253], off offset:32
	global_load_dwordx4 v[232:235], v[252:253], off offset:48
	s_mov_b64 s[98:99], 0x10000
	v_lshl_add_u64 v[252:253], v[252:253], 0, s[98:99]
	global_load_dwordx4 v[236:239], v[252:253], off
	global_load_dwordx4 v[240:243], v[252:253], off offset:16
	global_load_dwordx4 v[244:247], v[252:253], off offset:32
	global_load_dwordx4 v[248:251], v[252:253], off offset:48
	v_mov_b32_e32 v215, 0
	v_lshlrev_b64 v[216:217], 11, v[182:183]
	v_cmp_eq_u32_e32 vcc, 0, v179
	v_lshl_add_u64 v[216:217], s[24:25], 0, v[216:217]
	v_lshl_add_u64 v[218:219], v[180:181], 1, v[216:217]
	v_mov_b32_e32 v217, 0
	v_mov_b32_e32 v216, 0
	s_lshl_b32 s34, s15, 2
	s_ashr_i32 s35, s34, 31
	s_waitcnt vmcnt(23)
	v_pk_add_f32 v[200:201], v[116:117], v[200:201]
	v_pk_add_f32 v[198:199], v[114:115], v[198:199]
	s_waitcnt vmcnt(22)
	v_pk_add_f32 v[118:119], v[118:119], v[202:203]
	s_waitcnt vmcnt(21)
	v_pk_add_f32 v[128:129], v[128:129], v[208:209]
	v_pk_add_f32 v[126:127], v[126:127], v[206:207]
	s_waitcnt vmcnt(20)
	v_pk_add_f32 v[122:123], v[122:123], v[210:211]
	v_mul_f32_e32 v179, v199, v199
	v_mul_f32_e32 v202, v201, v201
	v_mul_f32_e32 v203, v119, v119
	v_cvt_pk_bf16_f32 v114, v198, v199
	v_cvt_pk_bf16_f32 v115, v200, v201
	v_cvt_pk_bf16_f32 v116, v118, v119
	v_cvt_pk_fp8_f32 v214, v198, v199
	v_cvt_pk_fp8_f32 v215, v118, v119
	v_mul_f32_e32 v119, v127, v127
	v_mul_f32_e32 v199, v129, v129
	v_pk_add_f32 v[120:121], v[120:121], v[204:205]
	v_pk_add_f32 v[124:125], v[124:125], v[212:213]
	v_cvt_pk_bf16_f32 v117, v120, v121
	v_mul_f32_e32 v205, v123, v123
	v_fmac_f32_e32 v179, v198, v198
	v_fmac_f32_e32 v202, v200, v200
	v_fmac_f32_e32 v119, v126, v126
	v_fmac_f32_e32 v199, v128, v128
	v_mul_f32_e32 v204, v121, v121
	v_mul_f32_e32 v206, v125, v125
	v_fmac_f32_e32 v203, v118, v118
	global_store_dwordx4 v[218:219], v[114:117], off
	v_fmac_f32_e32 v205, v122, v122
	v_add_f32_e32 v118, v119, v199
	v_add_f32_e32 v117, v179, v202
	v_fmac_f32_e32 v204, v120, v120
	v_fmac_f32_e32 v206, v124, v124
	v_add_f32_e32 v117, v117, v203
	v_add_f32_e32 v118, v118, v205
	v_add_f32_e32 v117, v204, v117
	v_add_f32_e32 v118, v206, v118
	v_and_b32_e32 v119, 64, v197
	v_add_f32_e32 v118, v117, v118
	v_xor_b32_e32 v117, 16, v197
	v_add_u32_e32 v119, 64, v119
	v_cmp_lt_i32_e64 s[2:3], v117, v119
	v_cvt_pk_bf16_f32 v114, v126, v127
	v_cvt_pk_bf16_f32 v115, v128, v129
	v_cvt_pk_bf16_f32 v116, v122, v123
	v_cvt_pk_fp8_f32 v217, v122, v123
	v_cvt_pk_fp8_f32 v215, v120, v121 op_sel:[0,0,1]
	v_cndmask_b32_e64 v117, v197, v117, s[2:3]
	v_lshlrev_b32_e32 v122, 2, v117
	ds_bpermute_b32 v120, v122, v118
	v_cvt_pk_bf16_f32 v117, v124, v125
	global_store_dwordx4 v[218:219], v[114:117], off offset:16
	v_cvt_pk_fp8_f32 v216, v126, v127
	v_cvt_pk_fp8_f32 v214, v200, v201 op_sel:[0,0,1]
	v_xor_b32_e32 v115, 32, v197
	v_cmp_lt_i32_e64 s[2:3], v115, v119
	s_waitcnt lgkmcnt(0)
	v_add_f32_e32 v114, v118, v120
	v_cvt_pk_fp8_f32 v216, v128, v129 op_sel:[0,0,1]
	v_cndmask_b32_e64 v115, v197, v115, s[2:3]
	v_lshlrev_b32_e32 v123, 2, v115
	ds_bpermute_b32 v115, v123, v114
	v_cvt_pk_fp8_f32 v217, v124, v125 op_sel:[0,0,1]
	v_lshlrev_b64 v[116:117], 10, v[182:183]
	v_lshl_add_u64 v[116:117], s[28:29], 0, v[116:117]
	v_lshl_add_u64 v[116:117], v[116:117], 0, v[180:181]
	global_store_dwordx4 v[116:117], v[214:217], off
	s_and_saveexec_b64 s[2:3], vcc
	s_cbranch_execz .LBB0_556
	v_lshlrev_b64 v[116:117], 6, v[182:183]
	v_lshl_add_u64 v[116:117], s[26:27], 0, v[116:117]
	v_lshl_add_u64 v[116:117], s[34:35], 2, v[116:117]
	s_lshl_b32 s20, s7, 2
	v_lshl_add_u64 v[116:117], v[116:117], 0, s[20:21]
	s_waitcnt lgkmcnt(0)
	v_add_f32_e32 v114, v114, v115
	global_store_dword v[116:117], v114, off
; __device__ __forceinline__ unsigned cvt_pk_bf16(float lo, float hi) { unsigned r; asm volatile("v_cvt_pk_bf16_f32 %0, %1, %2" : "=v"(r) : "v"(lo), "v"(hi)); return r; }
; __device__ __forceinline__ unsigned pk4_fp8(float a, float b, float c, float d) { int w = __builtin_amdgcn_cvt_pk_fp8_f32(a, b, 0, false); w = __builtin_amdgcn_cvt_pk_fp8_f32(c, d, w, true); return (unsigned)w; }
;     __device__ __forceinline__ void operator()(const f32x4 (&acc)[2][2][4][2], const pg8::Unit& u, int wr, int wc, int fr, int fq) const {
;     ...
;             for (int m = 0; m < 4; ++m) { const int row = row0 + ai * 128 + m * 16; float ss = 0.f;
;                 u32x4 q;
; #pragma unroll
;                 for (int bj = 0; bj < 2; ++bj) { const size_t off = (size_t)row * D + col0 + bj * 8;
;                     const float asc = BASE_F32 ? 1.0f : (1.0f / 256.0f);
;                     const f32x4 v0 = acc[ai][bj][m][0] * asc + b0[m][bj], v1 = acc[ai][bj][m][1] * asc + b1[m][bj];
;                     ss += (v0[0] * v0[0] + v0[1] * v0[1]) + (v0[2] * v0[2] + v0[3] * v0[3]) + (v1[0] * v1[0] + v1[1] * v1[1]) + (v1[2] * v1[2] + v1[3] * v1[3]);
;                     u32x4 w; w.x = cvt_pk_bf16(v0[0], v0[1]); w.y = cvt_pk_bf16(v0[2], v0[3]); w.z = cvt_pk_bf16(v1[0], v1[1]); w.w = cvt_pk_bf16(v1[2], v1[3]);
;                     *(u32x4*)(out + off) = w;
;                     if (BASE_F32) { const unsigned qa = pk4_fp8(v0[0], v0[1], v0[2], v0[3]), qb = pk4_fp8(v1[0], v1[1], v1[2], v1[3]); if (bj == 0) { q.x = qa; q.y = qb; } else { q.z = qa; q.w = qb; } } }
;                 if (BASE_F32) *(u32x4*)(q8 + (size_t)row * D + col0) = q;
;                 ss += __shfl_xor(ss, 16); ss += __shfl_xor(ss, 32);
;                 if (fq == 0) ssq[(size_t)row * 16 + u.pn * 4 + wc] = ss; }
.LBB0_556:
	s_or_b64 exec, exec, s[2:3]
	s_waitcnt vmcnt(19)
	v_pk_add_f32 v[112:113], v[112:113], v[176:177]
	v_pk_add_f32 v[116:117], v[110:111], v[174:175]
	v_pk_add_f32 v[120:121], v[106:107], v[170:171]
	v_mul_f32_e32 v106, v117, v117
	v_mul_f32_e32 v107, v113, v113
	v_fmac_f32_e32 v106, v116, v116
	v_fmac_f32_e32 v107, v112, v112
	v_add_f32_e32 v106, v106, v107
	v_mul_f32_e32 v107, v121, v121
	v_pk_add_f32 v[118:119], v[108:109], v[172:173]
	v_fmac_f32_e32 v107, v120, v120
	s_waitcnt lgkmcnt(0)
	v_lshlrev_b64 v[114:115], 11, v[190:191]
	v_add_f32_e32 v106, v106, v107
	v_mul_f32_e32 v107, v119, v119
	v_fmac_f32_e32 v107, v118, v118
	v_lshl_add_u64 v[114:115], s[24:25], 0, v[114:115]
	v_add_f32_e32 v124, v107, v106
	v_cvt_pk_bf16_f32 v106, v116, v117
	v_cvt_pk_bf16_f32 v107, v112, v113
	v_cvt_pk_bf16_f32 v108, v120, v121
	v_cvt_pk_bf16_f32 v109, v118, v119
	v_lshl_add_u64 v[114:115], v[180:181], 1, v[114:115]
	v_pk_add_f32 v[104:105], v[104:105], v[168:169]
	v_pk_add_f32 v[102:103], v[102:103], v[166:167]
	global_store_dwordx4 v[114:115], v[106:109], off
	v_mov_b32_e32 v110, 0
	v_cvt_pk_fp8_f32 v110, v116, v117
	v_pk_add_f32 v[108:109], v[98:99], v[162:163]
	v_mul_f32_e32 v98, v103, v103
	v_mul_f32_e32 v99, v105, v105
	v_fmac_f32_e32 v98, v102, v102
	v_fmac_f32_e32 v99, v104, v104
	v_add_f32_e32 v98, v98, v99
	v_mul_f32_e32 v99, v109, v109
	v_pk_add_f32 v[106:107], v[100:101], v[164:165]
	v_fmac_f32_e32 v99, v108, v108
	v_add_f32_e32 v98, v98, v99
	v_mul_f32_e32 v99, v107, v107
	v_fmac_f32_e32 v99, v106, v106
	v_add_f32_e32 v98, v99, v98
	v_cvt_pk_fp8_f32 v110, v112, v113 op_sel:[0,0,1]
	v_add_f32_e32 v116, v124, v98
	v_mov_b32_e32 v112, 0
	v_cvt_pk_bf16_f32 v98, v102, v103
	v_cvt_pk_fp8_f32 v112, v102, v103
	ds_bpermute_b32 v102, v122, v116
	v_mov_b32_e32 v111, 0
	v_mov_b32_e32 v113, 0
	v_cvt_pk_fp8_f32 v111, v120, v121
	v_cvt_pk_fp8_f32 v113, v108, v109
	v_cvt_pk_bf16_f32 v99, v104, v105
	v_cvt_pk_bf16_f32 v100, v108, v109
	v_cvt_pk_bf16_f32 v101, v106, v107
	global_store_dwordx4 v[114:115], v[98:101], off offset:16
	v_cvt_pk_fp8_f32 v111, v118, v119 op_sel:[0,0,1]
	v_cvt_pk_fp8_f32 v112, v104, v105 op_sel:[0,0,1]
	s_waitcnt lgkmcnt(0)
	v_add_f32_e32 v98, v116, v102
	ds_bpermute_b32 v99, v123, v98
	v_cvt_pk_fp8_f32 v113, v106, v107 op_sel:[0,0,1]
	v_lshlrev_b64 v[100:101], 10, v[190:191]
	v_lshl_add_u64 v[100:101], s[28:29], 0, v[100:101]
	v_lshl_add_u64 v[100:101], v[100:101], 0, v[180:181]
	global_store_dwordx4 v[100:101], v[110:113], off
	s_and_saveexec_b64 s[2:3], vcc
	s_cbranch_execz .LBB0_558
	v_lshlrev_b64 v[100:101], 6, v[190:191]
	v_lshl_add_u64 v[100:101], s[26:27], 0, v[100:101]
	v_lshl_add_u64 v[100:101], s[34:35], 2, v[100:101]
	s_lshl_b32 s20, s7, 2
	v_lshl_add_u64 v[100:101], v[100:101], 0, s[20:21]
	s_waitcnt lgkmcnt(0)
	v_add_f32_e32 v98, v98, v99
	global_store_dword v[100:101], v98, off
.LBB0_558:
	s_or_b64 exec, exec, s[2:3]
	s_waitcnt vmcnt(18)
	v_pk_add_f32 v[96:97], v[96:97], v[160:161]
	v_pk_add_f32 v[100:101], v[94:95], v[158:159]
	v_pk_add_f32 v[104:105], v[90:91], v[154:155]
	v_mul_f32_e32 v90, v101, v101
	v_mul_f32_e32 v91, v97, v97
	v_fmac_f32_e32 v90, v100, v100
	v_fmac_f32_e32 v91, v96, v96
	v_add_f32_e32 v90, v90, v91
	v_mul_f32_e32 v91, v105, v105
	v_pk_add_f32 v[102:103], v[92:93], v[156:157]
	v_fmac_f32_e32 v91, v104, v104
	s_waitcnt lgkmcnt(0)
	v_lshlrev_b64 v[98:99], 11, v[188:189]
	v_add_f32_e32 v90, v90, v91
	v_mul_f32_e32 v91, v103, v103
	v_fmac_f32_e32 v91, v102, v102
	v_lshl_add_u64 v[98:99], s[24:25], 0, v[98:99]
	v_add_f32_e32 v106, v91, v90
	v_cvt_pk_bf16_f32 v90, v100, v101
	v_cvt_pk_bf16_f32 v91, v96, v97
	v_cvt_pk_bf16_f32 v92, v104, v105
	v_cvt_pk_bf16_f32 v93, v102, v103
	v_lshl_add_u64 v[98:99], v[180:181], 1, v[98:99]
	v_pk_add_f32 v[88:89], v[88:89], v[152:153]
	v_pk_add_f32 v[86:87], v[86:87], v[150:151]
	global_store_dwordx4 v[98:99], v[90:93], off
	v_mov_b32_e32 v94, 0
	v_cvt_pk_fp8_f32 v94, v100, v101
	v_pk_add_f32 v[92:93], v[82:83], v[146:147]
	v_mul_f32_e32 v82, v87, v87
	v_mul_f32_e32 v83, v89, v89
	v_fmac_f32_e32 v82, v86, v86
	v_fmac_f32_e32 v83, v88, v88
	v_add_f32_e32 v82, v82, v83
	v_mul_f32_e32 v83, v93, v93
	v_pk_add_f32 v[90:91], v[84:85], v[148:149]
	v_fmac_f32_e32 v83, v92, v92
	v_add_f32_e32 v82, v82, v83
	v_mul_f32_e32 v83, v91, v91
	v_fmac_f32_e32 v83, v90, v90
	v_add_f32_e32 v82, v83, v82
	v_cvt_pk_fp8_f32 v94, v96, v97 op_sel:[0,0,1]
	v_add_f32_e32 v100, v106, v82
	v_mov_b32_e32 v96, 0
	v_cvt_pk_bf16_f32 v82, v86, v87
	v_cvt_pk_fp8_f32 v96, v86, v87
	ds_bpermute_b32 v86, v122, v100
	v_mov_b32_e32 v95, 0
	v_mov_b32_e32 v97, 0
	v_cvt_pk_fp8_f32 v95, v104, v105
	v_cvt_pk_fp8_f32 v97, v92, v93
	v_cvt_pk_bf16_f32 v83, v88, v89
	v_cvt_pk_bf16_f32 v84, v92, v93
	v_cvt_pk_bf16_f32 v85, v90, v91
	global_store_dwordx4 v[98:99], v[82:85], off offset:16
	v_cvt_pk_fp8_f32 v95, v102, v103 op_sel:[0,0,1]
	v_cvt_pk_fp8_f32 v96, v88, v89 op_sel:[0,0,1]
	s_waitcnt lgkmcnt(0)
	v_add_f32_e32 v82, v100, v86
	ds_bpermute_b32 v83, v123, v82
	v_cvt_pk_fp8_f32 v97, v90, v91 op_sel:[0,0,1]
	v_lshlrev_b64 v[84:85], 10, v[188:189]
	v_lshl_add_u64 v[84:85], s[28:29], 0, v[84:85]
	v_lshl_add_u64 v[84:85], v[84:85], 0, v[180:181]
	global_store_dwordx4 v[84:85], v[94:97], off
	s_and_saveexec_b64 s[2:3], vcc
	s_cbranch_execz .LBB0_560
	v_lshlrev_b64 v[84:85], 6, v[188:189]
	v_lshl_add_u64 v[84:85], s[26:27], 0, v[84:85]
	v_lshl_add_u64 v[84:85], s[34:35], 2, v[84:85]
	s_lshl_b32 s20, s7, 2
	v_lshl_add_u64 v[84:85], v[84:85], 0, s[20:21]
	s_waitcnt lgkmcnt(0)
	v_add_f32_e32 v82, v82, v83
	global_store_dword v[84:85], v82, off
; __device__ __forceinline__ unsigned cvt_pk_bf16(float lo, float hi) { unsigned r; asm volatile("v_cvt_pk_bf16_f32 %0, %1, %2" : "=v"(r) : "v"(lo), "v"(hi)); return r; }
; __device__ __forceinline__ unsigned pk4_fp8(float a, float b, float c, float d) { int w = __builtin_amdgcn_cvt_pk_fp8_f32(a, b, 0, false); w = __builtin_amdgcn_cvt_pk_fp8_f32(c, d, w, true); return (unsigned)w; }
;     __device__ __forceinline__ void operator()(const f32x4 (&acc)[2][2][4][2], const pg8::Unit& u, int wr, int wc, int fr, int fq) const {
;     ...
;             for (int m = 0; m < 4; ++m) { const int row = row0 + ai * 128 + m * 16; float ss = 0.f;
;                 u32x4 q;
; #pragma unroll
;                 for (int bj = 0; bj < 2; ++bj) { const size_t off = (size_t)row * D + col0 + bj * 8;
;                     const float asc = BASE_F32 ? 1.0f : (1.0f / 256.0f);
;                     const f32x4 v0 = acc[ai][bj][m][0] * asc + b0[m][bj], v1 = acc[ai][bj][m][1] * asc + b1[m][bj];
;                     ss += (v0[0] * v0[0] + v0[1] * v0[1]) + (v0[2] * v0[2] + v0[3] * v0[3]) + (v1[0] * v1[0] + v1[1] * v1[1]) + (v1[2] * v1[2] + v1[3] * v1[3]);
;                     u32x4 w; w.x = cvt_pk_bf16(v0[0], v0[1]); w.y = cvt_pk_bf16(v0[2], v0[3]); w.z = cvt_pk_bf16(v1[0], v1[1]); w.w = cvt_pk_bf16(v1[2], v1[3]);
;                     *(u32x4*)(out + off) = w;
;                     if (BASE_F32) { const unsigned qa = pk4_fp8(v0[0], v0[1], v0[2], v0[3]), qb = pk4_fp8(v1[0], v1[1], v1[2], v1[3]); if (bj == 0) { q.x = qa; q.y = qb; } else { q.z = qa; q.w = qb; } } }
;                 if (BASE_F32) *(u32x4*)(q8 + (size_t)row * D + col0) = q;
;                 ss += __shfl_xor(ss, 16); ss += __shfl_xor(ss, 32);
;                 if (fq == 0) ssq[(size_t)row * 16 + u.pn * 4 + wc] = ss; }
.LBB0_560:
	s_or_b64 exec, exec, s[2:3]
	s_waitcnt vmcnt(17)
	v_pk_add_f32 v[80:81], v[80:81], v[144:145]
	v_pk_add_f32 v[84:85], v[78:79], v[142:143]
	v_pk_add_f32 v[88:89], v[74:75], v[138:139]
	v_mul_f32_e32 v74, v85, v85
	v_mul_f32_e32 v75, v81, v81
	v_fmac_f32_e32 v74, v84, v84
	v_fmac_f32_e32 v75, v80, v80
	v_add_f32_e32 v74, v74, v75
	v_mul_f32_e32 v75, v89, v89
	v_pk_add_f32 v[86:87], v[76:77], v[140:141]
	v_fmac_f32_e32 v75, v88, v88
	s_waitcnt lgkmcnt(0)
	v_lshlrev_b64 v[82:83], 11, v[186:187]
	v_add_f32_e32 v74, v74, v75
	v_mul_f32_e32 v75, v87, v87
	v_fmac_f32_e32 v75, v86, v86
	v_lshl_add_u64 v[82:83], s[24:25], 0, v[82:83]
	v_add_f32_e32 v90, v75, v74
	v_cvt_pk_bf16_f32 v74, v84, v85
	v_cvt_pk_bf16_f32 v75, v80, v81
	v_cvt_pk_bf16_f32 v76, v88, v89
	v_cvt_pk_bf16_f32 v77, v86, v87
	v_lshl_add_u64 v[82:83], v[180:181], 1, v[82:83]
	v_pk_add_f32 v[72:73], v[72:73], v[136:137]
	v_pk_add_f32 v[70:71], v[70:71], v[134:135]
	global_store_dwordx4 v[82:83], v[74:77], off
	v_mov_b32_e32 v78, 0
	v_cvt_pk_fp8_f32 v78, v84, v85
	v_pk_add_f32 v[76:77], v[66:67], v[130:131]
	v_mul_f32_e32 v66, v71, v71
	v_mul_f32_e32 v67, v73, v73
	v_fmac_f32_e32 v66, v70, v70
	v_fmac_f32_e32 v67, v72, v72
	v_add_f32_e32 v66, v66, v67
	v_mul_f32_e32 v67, v77, v77
	v_pk_add_f32 v[74:75], v[68:69], v[132:133]
	v_fmac_f32_e32 v67, v76, v76
	v_add_f32_e32 v66, v66, v67
	v_mul_f32_e32 v67, v75, v75
	v_fmac_f32_e32 v67, v74, v74
	v_add_f32_e32 v66, v67, v66
	v_cvt_pk_fp8_f32 v78, v80, v81 op_sel:[0,0,1]
	v_add_f32_e32 v84, v90, v66
	v_mov_b32_e32 v80, 0
	v_cvt_pk_bf16_f32 v66, v70, v71
	v_cvt_pk_fp8_f32 v80, v70, v71
	ds_bpermute_b32 v70, v122, v84
	v_mov_b32_e32 v79, 0
	v_mov_b32_e32 v81, 0
	v_cvt_pk_fp8_f32 v79, v88, v89
	v_cvt_pk_fp8_f32 v81, v76, v77
	v_cvt_pk_bf16_f32 v67, v72, v73
	v_cvt_pk_bf16_f32 v68, v76, v77
	v_cvt_pk_bf16_f32 v69, v74, v75
	global_store_dwordx4 v[82:83], v[66:69], off offset:16
	v_cvt_pk_fp8_f32 v79, v86, v87 op_sel:[0,0,1]
	v_cvt_pk_fp8_f32 v80, v72, v73 op_sel:[0,0,1]
	s_waitcnt lgkmcnt(0)
	v_add_f32_e32 v66, v84, v70
	ds_bpermute_b32 v67, v123, v66
	v_cvt_pk_fp8_f32 v81, v74, v75 op_sel:[0,0,1]
	v_lshlrev_b64 v[68:69], 10, v[186:187]
	v_lshl_add_u64 v[68:69], s[28:29], 0, v[68:69]
	v_lshl_add_u64 v[68:69], v[68:69], 0, v[180:181]
	global_store_dwordx4 v[68:69], v[78:81], off
	s_and_saveexec_b64 s[2:3], vcc
	s_cbranch_execz .LBB0_562
	v_lshlrev_b64 v[68:69], 6, v[186:187]
	v_lshl_add_u64 v[68:69], s[26:27], 0, v[68:69]
	v_lshl_add_u64 v[68:69], s[34:35], 2, v[68:69]
	s_lshl_b32 s20, s7, 2
	v_lshl_add_u64 v[68:69], v[68:69], 0, s[20:21]
	s_waitcnt lgkmcnt(0)
	v_add_f32_e32 v66, v66, v67
	global_store_dword v[68:69], v66, off
; __device__ __forceinline__ unsigned cvt_pk_bf16(float lo, float hi) { unsigned r; asm volatile("v_cvt_pk_bf16_f32 %0, %1, %2" : "=v"(r) : "v"(lo), "v"(hi)); return r; }
;     __device__ __forceinline__ void operator()(const f32x4 (&acc)[2][2][4][2], const pg8::Unit& u, int wr, int wc, int fr, int fq) const {
;     ...
;             f32x4 b0[4][2], b1[4][2];
; #pragma unroll
;             for (int m = 0; m < 4; ++m)
; #pragma unroll
;                 for (int bj = 0; bj < 2; ++bj) { const size_t off = (size_t)(row0 + ai * 128 + m * 16) * D + col0 + bj * 8;
;                     if (BASE_F32) { b0[m][bj] = *(const f32x4*)((const float*)base + off); b1[m][bj] = *(const f32x4*)((const float*)base + off + 4); }
;                     else { const u32x4 w = *(const u32x4*)((const bf16*)base + off); b0[m][bj] = (f32x4){bflo(w.x), bfhi(w.x), bflo(w.y), bfhi(w.y)}; b1[m][bj] = (f32x4){bflo(w.z), bfhi(w.z), bflo(w.w), bfhi(w.w)}; } }
;             asm volatile("" ::: "memory");
; #pragma unroll
;             for (int m = 0; m < 4; ++m) { const int row = row0 + ai * 128 + m * 16; float ss = 0.f;
;                 u32x4 q;
; #pragma unroll
;                 for (int bj = 0; bj < 2; ++bj) { const size_t off = (size_t)row * D + col0 + bj * 8;
;                     const float asc = BASE_F32 ? 1.0f : (1.0f / 256.0f);
;                     const f32x4 v0 = acc[ai][bj][m][0] * asc + b0[m][bj], v1 = acc[ai][bj][m][1] * asc + b1[m][bj];
;                     ss += (v0[0] * v0[0] + v0[1] * v0[1]) + (v0[2] * v0[2] + v0[3] * v0[3]) + (v1[0] * v1[0] + v1[1] * v1[1]) + (v1[2] * v1[2] + v1[3] * v1[3]);
;                     u32x4 w; w.x = cvt_pk_bf16(v0[0], v0[1]); w.y = cvt_pk_bf16(v0[2], v0[3]); w.z = cvt_pk_bf16(v1[0], v1[1]); w.w = cvt_pk_bf16(v1[2], v1[3]);
;                     *(u32x4*)(out + off) = w;
;                     if (BASE_F32) { const unsigned qa = pk4_fp8(v0[0], v0[1], v0[2], v0[3]), qb = pk4_fp8(v1[0], v1[1], v1[2], v1[3]); if (bj == 0) { q.x = qa; q.y = qb; } else { q.z = qa; q.w = qb; } } }
;                 if (BASE_F32) *(u32x4*)(q8 + (size_t)row * D + col0) = q;
;                 ss += __shfl_xor(ss, 16); ss += __shfl_xor(ss, 32);
;                 if (fq == 0) ssq[(size_t)row * 16 + u.pn * 4 + wc] = ss; }
.LBB0_562:
	s_or_b64 exec, exec, s[2:3]
	v_add_u32_e32 v120, 0x80, v182
	v_ashrrev_i32_e32 v121, 31, v120
	s_waitcnt lgkmcnt(0)
	v_lshlrev_b64 v[66:67], 12, v[120:121]
	v_lshl_add_u64 v[66:67], v[184:185], 0, v[66:67]
	s_waitcnt vmcnt(12)
	v_mov_b64_e32 v[124:125], v[220:221]
	v_mov_b64_e32 v[126:127], v[222:223]
	v_mov_b64_e32 v[128:129], v[224:225]
	v_mov_b64_e32 v[130:131], v[226:227]
	v_mov_b64_e32 v[132:133], v[228:229]
	v_mov_b64_e32 v[134:135], v[230:231]
	v_mov_b64_e32 v[136:137], v[232:233]
	v_mov_b64_e32 v[138:139], v[234:235]
	v_add_u32_e32 v118, 0x90, v182
	v_add_u32_e32 v116, 0xa0, v182
	v_add_u32_e32 v114, 0xb0, v182
	v_ashrrev_i32_e32 v119, 31, v118
	v_ashrrev_i32_e32 v117, 31, v116
	v_ashrrev_i32_e32 v115, 31, v114
	v_lshlrev_b64 v[66:67], 12, v[118:119]
	v_lshlrev_b64 v[68:69], 12, v[116:117]
	v_lshlrev_b64 v[70:71], 12, v[114:115]
	v_lshl_add_u64 v[66:67], v[184:185], 0, v[66:67]
	v_lshl_add_u64 v[68:69], v[184:185], 0, v[68:69]
	v_lshl_add_u64 v[78:79], v[184:185], 0, v[70:71]
	v_mov_b64_e32 v[98:99], v[248:249]
	v_mov_b64_e32 v[100:101], v[250:251]
	v_mov_b64_e32 v[102:103], v[244:245]
	v_mov_b64_e32 v[104:105], v[246:247]
	v_mov_b64_e32 v[106:107], v[240:241]
	v_mov_b64_e32 v[108:109], v[242:243]
	v_mov_b64_e32 v[110:111], v[236:237]
	v_mov_b64_e32 v[112:113], v[238:239]
	global_load_dwordx4 v[82:85], v[68:69], off offset:48
	global_load_dwordx4 v[86:89], v[68:69], off offset:32
	global_load_dwordx4 v[90:93], v[68:69], off offset:16
	global_load_dwordx4 v[94:97], v[68:69], off
	s_nop 0
	global_load_dwordx4 v[66:69], v[78:79], off offset:48
	global_load_dwordx4 v[70:73], v[78:79], off offset:32
	global_load_dwordx4 v[74:77], v[78:79], off offset:16
	s_nop 0
	global_load_dwordx4 v[78:81], v[78:79], off
	v_mov_b32_e32 v140, 0
	v_mov_b32_e32 v141, 0
	v_lshlrev_b64 v[144:145], 11, v[120:121]
	v_lshl_add_u64 v[144:145], s[24:25], 0, v[144:145]
	v_lshl_add_u64 v[144:145], v[180:181], 1, v[144:145]
	v_mov_b32_e32 v142, 0
	v_mov_b32_e32 v143, 0
	s_waitcnt vmcnt(15)
	v_pk_add_f32 v[126:127], v[52:53], v[126:127]
	v_pk_add_f32 v[124:125], v[50:51], v[124:125]
	s_waitcnt vmcnt(14)
	v_pk_add_f32 v[54:55], v[54:55], v[128:129]
	s_waitcnt vmcnt(13)
	v_pk_add_f32 v[60:61], v[60:61], v[134:135]
	v_pk_add_f32 v[58:59], v[58:59], v[132:133]
	v_pk_add_f32 v[56:57], v[56:57], v[130:131]
	s_waitcnt vmcnt(12)
	v_pk_add_f32 v[62:63], v[62:63], v[136:137]
	v_mul_f32_e32 v128, v125, v125
	v_mul_f32_e32 v129, v127, v127
	v_mul_f32_e32 v130, v55, v55
	v_cvt_pk_bf16_f32 v50, v124, v125
	v_cvt_pk_bf16_f32 v51, v126, v127
	v_cvt_pk_bf16_f32 v52, v54, v55
	v_cvt_pk_fp8_f32 v140, v124, v125
	v_cvt_pk_fp8_f32 v141, v54, v55
	v_mul_f32_e32 v55, v59, v59
	v_mul_f32_e32 v125, v61, v61
	v_pk_add_f32 v[64:65], v[64:65], v[138:139]
	v_cvt_pk_bf16_f32 v53, v56, v57
	v_mul_f32_e32 v132, v63, v63
	v_fmac_f32_e32 v128, v124, v124
	v_fmac_f32_e32 v129, v126, v126
	v_fmac_f32_e32 v55, v58, v58
	v_fmac_f32_e32 v125, v60, v60
	v_mul_f32_e32 v131, v57, v57
	v_mul_f32_e32 v133, v65, v65
	v_fmac_f32_e32 v130, v54, v54
	global_store_dwordx4 v[144:145], v[50:53], off
	v_fmac_f32_e32 v132, v62, v62
	v_add_f32_e32 v54, v55, v125
	v_add_f32_e32 v53, v128, v129
	v_fmac_f32_e32 v131, v56, v56
	v_fmac_f32_e32 v133, v64, v64
	v_add_f32_e32 v53, v53, v130
	v_add_f32_e32 v54, v54, v132
	v_add_f32_e32 v53, v131, v53
	v_add_f32_e32 v54, v133, v54
	v_add_f32_e32 v54, v53, v54
	ds_bpermute_b32 v55, v122, v54
	v_cvt_pk_fp8_f32 v142, v58, v59
	v_cvt_pk_fp8_f32 v143, v62, v63
	v_cvt_pk_bf16_f32 v50, v58, v59
	v_cvt_pk_bf16_f32 v51, v60, v61
	v_cvt_pk_bf16_f32 v52, v62, v63
	v_cvt_pk_bf16_f32 v53, v64, v65
	global_store_dwordx4 v[144:145], v[50:53], off offset:16
	v_cvt_pk_fp8_f32 v140, v126, v127 op_sel:[0,0,1]
	v_cvt_pk_fp8_f32 v141, v56, v57 op_sel:[0,0,1]
	s_waitcnt lgkmcnt(0)
	v_add_f32_e32 v50, v54, v55
	ds_bpermute_b32 v51, v123, v50
	v_cvt_pk_fp8_f32 v142, v60, v61 op_sel:[0,0,1]
	v_cvt_pk_fp8_f32 v143, v64, v65 op_sel:[0,0,1]
	v_lshlrev_b64 v[52:53], 10, v[120:121]
	v_lshl_add_u64 v[52:53], s[28:29], 0, v[52:53]
	v_lshl_add_u64 v[52:53], v[52:53], 0, v[180:181]
	global_store_dwordx4 v[52:53], v[140:143], off
	s_and_saveexec_b64 s[2:3], vcc
	s_cbranch_execz .LBB0_564
	v_lshlrev_b64 v[52:53], 6, v[120:121]
	v_lshl_add_u64 v[52:53], s[26:27], 0, v[52:53]
	v_lshl_add_u64 v[52:53], s[34:35], 2, v[52:53]
	s_lshl_b32 s20, s7, 2
	v_lshl_add_u64 v[52:53], v[52:53], 0, s[20:21]
	s_waitcnt lgkmcnt(0)
	v_add_f32_e32 v50, v50, v51
	global_store_dword v[52:53], v50, off
